# LN1 router logits: 64 serialized ds_read_b128->lgkmcnt(0) per row software-pipelined (12 reads in flight, rotating quads, counted lgkmcnt)
# speedup vs baseline: 1.0154x; 1.0154x over previous
; #define LAS __attribute__((address_space(3)))
; __device__ __forceinline__ unsigned pk2(float lo, float hi) { return (unsigned)f2bf(lo) | ((unsigned)f2bf(hi) << 16); }
; __device__ __forceinline__ float frsq(float x) { return __builtin_amdgcn_rsqf(x); }
; __device__ __forceinline__ void ln_affine(f32x4 (&v)[4], const LnPar& q) {
;     float s = 0.f;
; #pragma unroll
;     for (int j = 0; j < 4; ++j) s += (v[j][0] + v[j][1]) + (v[j][2] + v[j][3]);
;     const float mean = wave_sum(s) * (1.f / D); float s2 = 0.f;
; #pragma unroll
;     for (int j = 0; j < 4; ++j) { v[j] = v[j] - mean; s2 += (v[j][0] * v[j][0] + v[j][1] * v[j][1]) + (v[j][2] * v[j][2] + v[j][3] * v[j][3]); }
;     const float rstd = frsq(wave_sum(s2) * (1.f / D) + 1e-5f);
; #pragma unroll
;     for (int j = 0; j < 4; ++j) v[j] = v[j] * rstd * q.g[j] + q.b[j];
; }
; __device__ __forceinline__ void store_row_bf16(bf16_t* row, const f32x4 (&v)[4], int lane) {
; #pragma unroll
;     for (int j = 0; j < 4; ++j) { u32x2 w; w.x = pk2(v[j][0], v[j][1]); w.y = pk2(v[j][2], v[j][3]); *(u32x2*)(row + 4 * lane + 256 * j) = w; }
; }
; __device__ __forceinline__ void ph_ln1(const Params& p, int l, LAS unsigned char* lds, const int wvid) {
;     ...
;         ln_affine(v, ln1);
;         store_row_bf16(HB + (size_t)r * D, v, lane);
;         float lg[16];
; #pragma unroll
;         for (int e = 0; e < 16; ++e) lg[e] = 0.f;
; #pragma unroll
;         for (int j = 0; j < 4; ++j)
; #pragma unroll
;             for (int e = 0; e < 16; ++e) { const f32x4 w = *(const LAS f32x4*)(rw + e * D + 256 * j + 4 * lane);
;                 lg[e] += (v[j][0] * w[0] + v[j][1] * w[1]) + (v[j][2] * w[2] + v[j][3] * w[3]); }
.LBB0_1078:
	s_or_b64 exec, exec, s[0:1]
	v_pk_add_f32 v[64:65], v[66:67], v[34:35]
	v_add_f32_e32 v75, v62, v63
	v_add_f32_e32 v0, v64, v65
	v_pk_add_f32 v[64:65], v[68:69], v[36:37]
	v_add_f32_e32 v77, 0, v0
	v_pk_add_f32 v[64:65], v[64:65], v[64:65] op_sel_hi:[0,1]
	v_add_f32_e32 v79, v60, v61
	v_mov_b32_e32 v73, v65
	v_pk_add_f32 v[70:71], v[74:75], v[78:79]
	v_pk_add_f32 v[64:65], v[72:73], v[76:77]
	ds_read_b128 v[118:121], v39
	ds_read_b128 v[122:125], v39 offset:4096
	ds_read_b128 v[126:129], v39 offset:8192
	ds_read_b128 v[130:133], v39 offset:12288
	ds_read_b128 v[134:137], v39 offset:16384
	ds_read_b128 v[138:141], v39 offset:20480
	ds_read_b128 v[142:145], v39 offset:24576
	ds_read_b128 v[146:149], v39 offset:28672
	ds_read_b128 v[232:235], v39 offset:32768
	ds_read_b128 v[236:239], v39 offset:36864
	ds_read_b128 v[240:243], v39 offset:40960
	ds_read_b128 v[244:247], v39 offset:45056
	v_pk_add_f32 v[64:65], v[70:71], v[64:65]
	s_nop 0
	v_add_f32_e32 v0, v64, v65
	v_mov_b32_e32 v64, v1
	s_nop 0
	v_add_f32_dpp v0, v0, v0 quad_perm:[1,0,3,2] row_mask:0xf bank_mask:0xf bound_ctrl:1
	s_nop 1
	v_add_f32_dpp v0, v0, v0 quad_perm:[2,3,0,1] row_mask:0xf bank_mask:0xf bound_ctrl:1
	s_nop 1
	v_add_f32_dpp v0, v0, v0 row_half_mirror row_mask:0xf bank_mask:0xf bound_ctrl:1
	s_nop 1
	v_add_f32_dpp v0, v0, v0 row_mirror row_mask:0xf bank_mask:0xf bound_ctrl:1
	s_nop 1
	v_mov_b32_dpp v64, v0 row_bcast:15 row_mask:0xa bank_mask:0xf
	v_add_f32_e32 v0, v0, v64
	v_mov_b32_e32 v64, v1
	s_nop 1
	v_mov_b32_dpp v64, v0 row_bcast:31 row_mask:0xc bank_mask:0xf
	v_add_f32_e32 v0, v0, v64
	s_nop 0
	v_readlane_b32 s0, v0, 63
	s_nop 1
	v_fmac_f32_e32 v66, s0, v220
	v_fmac_f32_e32 v35, s0, v220
	v_fmac_f32_e32 v67, s0, v220
	v_fmac_f32_e32 v34, s0, v220
	v_mov_b32_e32 v64, v67
	v_mov_b32_e32 v65, v35
	v_mov_b32_e32 v35, v66
	v_pk_mul_f32 v[70:71], v[64:65], v[64:65]
	v_pk_mul_f32 v[66:67], v[34:35], v[34:35]
	v_fmac_f32_e32 v68, s0, v220
	v_fmac_f32_e32 v37, s0, v220
	v_fmac_f32_e32 v69, s0, v220
	v_pk_mov_b32 v[80:81], v[66:67], v[70:71] op_sel:[1,0]
	v_mov_b32_e32 v67, v71
	v_fmac_f32_e32 v36, s0, v220
	v_mov_b32_e32 v70, v69
	v_mov_b32_e32 v71, v37
	v_mov_b32_e32 v37, v68
	v_pk_add_f32 v[66:67], v[80:81], v[66:67]
	v_pk_mul_f32 v[80:81], v[70:71], v[70:71]
	v_pk_mul_f32 v[68:69], v[36:37], v[36:37]
	v_fmac_f32_e32 v62, s0, v220
	v_pk_mov_b32 v[82:83], v[68:69], v[80:81] op_sel:[1,0]
	v_mov_b32_e32 v69, v81
	v_fmac_f32_e32 v63, s0, v220
	v_fmac_f32_e32 v60, s0, v220
	v_mul_f32_e32 v0, v62, v62
	v_pk_add_f32 v[68:69], v[82:83], v[68:69]
	v_fmac_f32_e32 v61, s0, v220
	v_pk_fma_f32 v[80:81], v[62:63], v[62:63], v[0:1] op_sel_hi:[1,1,0]
	v_mul_f32_e32 v0, v60, v60
	v_pk_add_f32 v[66:67], v[66:67], v[66:67] op_sel_hi:[0,1]
	v_pk_add_f32 v[68:69], v[68:69], v[68:69] op_sel_hi:[0,1]
	v_pk_fma_f32 v[82:83], v[60:61], v[60:61], v[0:1] op_sel_hi:[1,1,0]
	v_fmac_f32_e32 v76, s0, v220
	v_fmac_f32_e32 v72, s0, v220
	v_fmac_f32_e32 v78, s0, v220
	v_fmac_f32_e32 v74, s0, v220
	v_mul_f32_e32 v80, v74, v74
	v_mul_f32_e32 v82, v78, v78
	v_mul_f32_e32 v66, v72, v72
	v_mul_f32_e32 v68, v76, v76
	v_pk_add_f32 v[80:81], v[80:81], v[82:83]
	v_pk_add_f32 v[66:67], v[66:67], v[68:69]
	v_mov_b32_e32 v75, v78
	v_pk_add_f32 v[66:67], v[80:81], v[66:67]
	v_mov_b32_e32 v73, v76
	v_add_f32_e32 v0, v66, v67
	v_mov_b32_e32 v66, v1
	s_nop 0
	v_add_f32_dpp v0, v0, v0 quad_perm:[1,0,3,2] row_mask:0xf bank_mask:0xf bound_ctrl:1
	s_nop 1
	v_add_f32_dpp v0, v0, v0 quad_perm:[2,3,0,1] row_mask:0xf bank_mask:0xf bound_ctrl:1
	s_nop 1
	v_add_f32_dpp v0, v0, v0 row_half_mirror row_mask:0xf bank_mask:0xf bound_ctrl:1
	s_nop 1
	v_add_f32_dpp v0, v0, v0 row_mirror row_mask:0xf bank_mask:0xf bound_ctrl:1
	s_nop 1
	v_mov_b32_dpp v66, v0 row_bcast:15 row_mask:0xa bank_mask:0xf
	v_add_f32_e32 v0, v0, v66
	v_mov_b32_e32 v66, v1
	s_nop 1
	v_mov_b32_dpp v66, v0 row_bcast:31 row_mask:0xc bank_mask:0xf
	v_add_f32_e32 v0, v0, v66
	s_nop 0
	v_readlane_b32 s0, v0, 63
	s_nop 1
	v_fma_f32 v0, s0, v221, v204
	v_rsq_f32_e32 v0, v0
	s_nop 0
	v_pk_mul_f32 v[34:35], v[34:35], v[0:1] op_sel_hi:[1,0]
	s_nop 0
	v_pk_fma_f32 v[94:95], v[30:31], v[34:35], v[22:23]
	v_pk_mul_f32 v[34:35], v[36:37], v[0:1] op_sel_hi:[1,0]
	v_pk_mul_f32 v[36:37], v[70:71], v[0:1] op_sel_hi:[1,0]
	v_pk_mul_f32 v[64:65], v[64:65], v[0:1] op_sel_hi:[1,0]
	v_pk_fma_f32 v[68:69], v[28:29], v[36:37], v[20:21]
	v_pk_fma_f32 v[70:71], v[26:27], v[34:35], v[18:19]
	v_pk_mul_f32 v[34:35], v[62:63], v[0:1] op_sel_hi:[1,0]
	v_pk_mul_f32 v[36:37], v[60:61], v[0:1] op_sel_hi:[1,0]
	v_pk_fma_f32 v[92:93], v[32:33], v[64:65], v[24:25]
	v_pk_fma_f32 v[64:65], v[16:17], v[36:37], v[8:9]
	v_pk_fma_f32 v[66:67], v[14:15], v[34:35], v[6:7]
	v_pk_mul_f32 v[34:35], v[74:75], v[0:1] op_sel_hi:[1,0]
	v_pk_mul_f32 v[36:37], v[72:73], v[0:1] op_sel_hi:[1,0]
	v_bfe_u32 v0, v94, 16, 1
	v_pk_fma_f32 v[62:63], v[10:11], v[34:35], v[2:3]
	v_add3_u32 v0, v94, v0, s79
	v_bfe_u32 v34, v95, 16, 1
	v_lshrrev_b32_e32 v0, 16, v0
	v_add3_u32 v34, v95, v34, s79
	v_and_or_b32 v34, v34, s89, v0
	v_bfe_u32 v0, v92, 16, 1
	v_add3_u32 v0, v92, v0, s79
	v_bfe_u32 v35, v93, 16, 1
	v_lshrrev_b32_e32 v0, 16, v0
	v_add3_u32 v35, v93, v35, s79
	v_and_or_b32 v35, v35, s89, v0
	v_bfe_u32 v0, v70, 16, 1
	global_store_dwordx2 v[58:59], v[34:35], off offset:-1536
	v_add3_u32 v0, v70, v0, s79
	v_bfe_u32 v34, v71, 16, 1
	v_lshrrev_b32_e32 v0, 16, v0
	v_add3_u32 v34, v71, v34, s79
	v_and_or_b32 v34, v34, s89, v0
	v_bfe_u32 v0, v68, 16, 1
	v_add3_u32 v0, v68, v0, s79
	v_bfe_u32 v35, v69, 16, 1
	v_lshrrev_b32_e32 v0, 16, v0
	v_add3_u32 v35, v69, v35, s79
	v_and_or_b32 v35, v35, s89, v0
	v_bfe_u32 v0, v66, 16, 1
	global_store_dwordx2 v[58:59], v[34:35], off offset:-1024
	v_add3_u32 v0, v66, v0, s79
	v_bfe_u32 v34, v67, 16, 1
	v_lshrrev_b32_e32 v0, 16, v0
	v_add3_u32 v34, v67, v34, s79
	v_and_or_b32 v34, v34, s89, v0
	v_bfe_u32 v0, v64, 16, 1
	v_add3_u32 v0, v64, v0, s79
	v_bfe_u32 v35, v65, 16, 1
	v_lshrrev_b32_e32 v0, 16, v0
	v_add3_u32 v35, v65, v35, s79
	v_and_or_b32 v35, v35, s89, v0
	v_bfe_u32 v0, v62, 16, 1
	global_store_dwordx2 v[58:59], v[34:35], off offset:-512
	v_add3_u32 v0, v62, v0, s79
	v_bfe_u32 v34, v63, 16, 1
	v_pk_fma_f32 v[60:61], v[12:13], v[36:37], v[4:5]
	v_lshrrev_b32_e32 v0, 16, v0
	v_add3_u32 v34, v63, v34, s79
	v_and_or_b32 v34, v34, s89, v0
	v_bfe_u32 v0, v60, 16, 1
	v_add3_u32 v0, v60, v0, s79
	v_bfe_u32 v35, v61, 16, 1
	v_lshrrev_b32_e32 v0, 16, v0
	v_add3_u32 v35, v61, v35, s79
	v_and_or_b32 v35, v35, s89, v0
	global_store_dwordx2 v[58:59], v[34:35], off
	s_waitcnt lgkmcnt(11)
; #define LAS __attribute__((address_space(3)))
; __device__ __forceinline__ void ph_ln1(const Params& p, int l, LAS unsigned char* lds, const int wvid) {
;     ...
; #pragma unroll
;         for (int j = 0; j < 4; ++j)
; #pragma unroll
;             for (int e = 0; e < 16; ++e) { const f32x4 w = *(const LAS f32x4*)(rw + e * D + 256 * j + 4 * lane);
;                 lg[e] += (v[j][0] * w[0] + v[j][1] * w[1]) + (v[j][2] * w[2] + v[j][3] * w[3]); }
	v_mul_f32_e32 v0, v119, v95
	v_fmac_f32_e32 v0, v118, v94
	v_mul_f32_e32 v34, v121, v93
	v_fmac_f32_e32 v34, v120, v92
	ds_read_b128 v[118:121], v39 offset:49152
	v_add_f32_e32 v0, v0, v34
	v_add_f32_e32 v72, 0, v0
	s_waitcnt lgkmcnt(11)
	v_mul_f32_e32 v0, v123, v95
	v_fmac_f32_e32 v0, v122, v94
	v_mul_f32_e32 v34, v125, v93
	v_fmac_f32_e32 v34, v124, v92
	ds_read_b128 v[122:125], v39 offset:53248
	v_add_f32_e32 v0, v0, v34
	v_add_f32_e32 v73, 0, v0
	s_waitcnt lgkmcnt(11)
	v_mul_f32_e32 v0, v95, v127
	v_fmac_f32_e32 v0, v94, v126
	v_mul_f32_e32 v34, v93, v129
	v_fmac_f32_e32 v34, v92, v128
	ds_read_b128 v[126:129], v39 offset:57344
	v_add_f32_e32 v0, v0, v34
	v_add_f32_e32 v75, 0, v0
	s_waitcnt lgkmcnt(11)
	v_mul_f32_e32 v0, v95, v131
	v_fmac_f32_e32 v0, v94, v130
	v_mul_f32_e32 v34, v93, v133
	v_fmac_f32_e32 v34, v92, v132
	ds_read_b128 v[130:133], v39 offset:61440
	v_add_f32_e32 v0, v0, v34
	v_add_f32_e32 v77, 0, v0
	s_waitcnt lgkmcnt(11)
	v_mul_f32_e32 v0, v95, v135
	v_fmac_f32_e32 v0, v94, v134
	v_mul_f32_e32 v34, v93, v137
	v_fmac_f32_e32 v34, v92, v136
	ds_read_b128 v[134:137], v39 offset:1024
	v_add_f32_e32 v0, v0, v34
	v_add_f32_e32 v79, 0, v0
	s_waitcnt lgkmcnt(11)
	v_mul_f32_e32 v0, v95, v139
	v_fmac_f32_e32 v0, v94, v138
	v_mul_f32_e32 v34, v93, v141
	v_fmac_f32_e32 v34, v92, v140
	ds_read_b128 v[138:141], v39 offset:5120
	v_add_f32_e32 v0, v0, v34
	v_add_f32_e32 v81, 0, v0
	s_waitcnt lgkmcnt(11)
	v_mul_f32_e32 v0, v95, v143
	v_fmac_f32_e32 v0, v94, v142
	v_mul_f32_e32 v34, v93, v145
	v_fmac_f32_e32 v34, v92, v144
	ds_read_b128 v[142:145], v39 offset:9216
	v_add_f32_e32 v0, v0, v34
	v_add_f32_e32 v82, 0, v0
	s_waitcnt lgkmcnt(11)
	v_mul_f32_e32 v0, v95, v147
	v_fmac_f32_e32 v0, v94, v146
	v_mul_f32_e32 v34, v93, v149
	v_fmac_f32_e32 v34, v92, v148
	ds_read_b128 v[146:149], v39 offset:13312
	v_add_f32_e32 v0, v0, v34
	v_add_f32_e32 v80, 0, v0
	s_waitcnt lgkmcnt(11)
	v_mul_f32_e32 v0, v95, v233
	v_fmac_f32_e32 v0, v94, v232
	v_mul_f32_e32 v34, v93, v235
	v_fmac_f32_e32 v34, v92, v234
	ds_read_b128 v[232:235], v39 offset:17408
	v_add_f32_e32 v0, v0, v34
	v_add_f32_e32 v78, 0, v0
	s_waitcnt lgkmcnt(11)
	v_mul_f32_e32 v0, v95, v237
	v_fmac_f32_e32 v0, v94, v236
	v_mul_f32_e32 v34, v93, v239
	v_fmac_f32_e32 v34, v92, v238
	ds_read_b128 v[236:239], v39 offset:21504
	v_add_f32_e32 v0, v0, v34
	v_add_f32_e32 v76, 0, v0
	s_waitcnt lgkmcnt(11)
	v_mul_f32_e32 v0, v95, v241
	v_fmac_f32_e32 v0, v94, v240
	v_mul_f32_e32 v34, v93, v243
	v_fmac_f32_e32 v34, v92, v242
	ds_read_b128 v[240:243], v39 offset:25600
	v_add_f32_e32 v0, v0, v34
	v_add_f32_e32 v74, 0, v0
	s_waitcnt lgkmcnt(11)
	v_mul_f32_e32 v0, v95, v245
	v_fmac_f32_e32 v0, v94, v244
	v_mul_f32_e32 v34, v93, v247
	v_fmac_f32_e32 v34, v92, v246
	ds_read_b128 v[244:247], v39 offset:29696
	v_add_f32_e32 v0, v0, v34
	v_add_f32_e32 v37, 0, v0
	s_waitcnt lgkmcnt(11)
	v_mul_f32_e32 v0, v95, v119
	v_mul_f32_e32 v34, v93, v121
	v_fmac_f32_e32 v0, v94, v118
	v_fmac_f32_e32 v34, v92, v120
	ds_read_b128 v[118:121], v39 offset:33792
	v_add_f32_e32 v0, v0, v34
	v_add_f32_e32 v36, 0, v0
	s_waitcnt lgkmcnt(11)
	v_mul_f32_e32 v0, v95, v123
	v_mul_f32_e32 v34, v93, v125
	v_fmac_f32_e32 v0, v94, v122
	v_fmac_f32_e32 v34, v92, v124
	ds_read_b128 v[122:125], v39 offset:37888
	v_add_f32_e32 v0, v0, v34
	v_add_f32_e32 v35, 0, v0
	s_waitcnt lgkmcnt(11)
	v_mul_f32_e32 v0, v95, v127
	v_mul_f32_e32 v34, v93, v129
	v_fmac_f32_e32 v0, v94, v126
	v_fmac_f32_e32 v34, v92, v128
	ds_read_b128 v[126:129], v39 offset:41984
	v_add_f32_e32 v0, v0, v34
	v_add_f32_e32 v34, 0, v0
	s_waitcnt lgkmcnt(11)
	v_mul_f32_e32 v0, v95, v131
	v_mul_f32_e32 v83, v93, v133
	v_fmac_f32_e32 v0, v94, v130
	v_fmac_f32_e32 v83, v92, v132
	ds_read_b128 v[130:133], v39 offset:46080
	v_add_f32_e32 v0, v0, v83
	v_add_f32_e32 v0, 0, v0
	s_waitcnt lgkmcnt(11)
	v_mul_f32_e32 v83, v71, v135
	v_fmac_f32_e32 v83, v70, v134
	v_mul_f32_e32 v88, v69, v137
	v_fmac_f32_e32 v88, v68, v136
	ds_read_b128 v[134:137], v39 offset:50176
	v_add_f32_e32 v83, v83, v88
	v_add_f32_e32 v72, v72, v83
	s_waitcnt lgkmcnt(11)
	v_mul_f32_e32 v83, v71, v139
	v_fmac_f32_e32 v83, v70, v138
	v_mul_f32_e32 v88, v69, v141
	v_fmac_f32_e32 v88, v68, v140
	ds_read_b128 v[138:141], v39 offset:54272
	v_add_f32_e32 v83, v83, v88
	v_add_f32_e32 v73, v73, v83
	s_waitcnt lgkmcnt(11)
	v_mul_f32_e32 v83, v71, v143
	v_fmac_f32_e32 v83, v70, v142
	v_mul_f32_e32 v88, v69, v145
	v_fmac_f32_e32 v88, v68, v144
	ds_read_b128 v[142:145], v39 offset:58368
	v_add_f32_e32 v83, v83, v88
	v_add_f32_e32 v75, v75, v83
	s_waitcnt lgkmcnt(11)
	v_mul_f32_e32 v83, v71, v147
	v_fmac_f32_e32 v83, v70, v146
	v_mul_f32_e32 v88, v69, v149
	v_fmac_f32_e32 v88, v68, v148
	ds_read_b128 v[146:149], v39 offset:62464
	v_add_f32_e32 v83, v83, v88
	v_add_f32_e32 v77, v77, v83
	s_waitcnt lgkmcnt(11)
	v_mul_f32_e32 v83, v71, v233
	v_fmac_f32_e32 v83, v70, v232
	v_mul_f32_e32 v88, v69, v235
	v_fmac_f32_e32 v88, v68, v234
	ds_read_b128 v[232:235], v39 offset:2048
	v_add_f32_e32 v83, v83, v88
	v_add_f32_e32 v79, v79, v83
	s_waitcnt lgkmcnt(11)
	v_mul_f32_e32 v83, v71, v237
	v_fmac_f32_e32 v83, v70, v236
	v_mul_f32_e32 v88, v69, v239
	v_fmac_f32_e32 v88, v68, v238
	ds_read_b128 v[236:239], v39 offset:6144
	v_add_f32_e32 v83, v83, v88
	v_add_f32_e32 v81, v81, v83
	s_waitcnt lgkmcnt(11)
	v_mul_f32_e32 v83, v71, v241
	v_fmac_f32_e32 v83, v70, v240
	v_mul_f32_e32 v88, v69, v243
	v_fmac_f32_e32 v88, v68, v242
	ds_read_b128 v[240:243], v39 offset:10240
	v_add_f32_e32 v83, v83, v88
	v_add_f32_e32 v82, v82, v83
	s_waitcnt lgkmcnt(11)
; #define LAS __attribute__((address_space(3)))
; __device__ __forceinline__ void ph_ln1(const Params& p, int l, LAS unsigned char* lds, const int wvid) {
;     ...
; #pragma unroll
;         for (int j = 0; j < 4; ++j)
; #pragma unroll
;             for (int e = 0; e < 16; ++e) { const f32x4 w = *(const LAS f32x4*)(rw + e * D + 256 * j + 4 * lane);
;                 lg[e] += (v[j][0] * w[0] + v[j][1] * w[1]) + (v[j][2] * w[2] + v[j][3] * w[3]); }
	v_mul_f32_e32 v83, v71, v245
	v_fmac_f32_e32 v83, v70, v244
	v_mul_f32_e32 v88, v69, v247
	v_fmac_f32_e32 v88, v68, v246
	ds_read_b128 v[244:247], v39 offset:14336
	v_add_f32_e32 v83, v83, v88
	v_add_f32_e32 v80, v80, v83
	s_waitcnt lgkmcnt(11)
	v_mul_f32_e32 v83, v71, v119
	v_fmac_f32_e32 v83, v70, v118
	v_mul_f32_e32 v88, v69, v121
	v_fmac_f32_e32 v88, v68, v120
	ds_read_b128 v[118:121], v39 offset:18432
	v_add_f32_e32 v83, v83, v88
	v_add_f32_e32 v78, v78, v83
	s_waitcnt lgkmcnt(11)
	v_mul_f32_e32 v83, v71, v123
	v_fmac_f32_e32 v83, v70, v122
	v_mul_f32_e32 v88, v69, v125
	v_fmac_f32_e32 v88, v68, v124
	ds_read_b128 v[122:125], v39 offset:22528
	v_add_f32_e32 v83, v83, v88
	v_add_f32_e32 v76, v76, v83
	s_waitcnt lgkmcnt(11)
	v_mul_f32_e32 v83, v71, v127
	v_fmac_f32_e32 v83, v70, v126
	v_mul_f32_e32 v88, v69, v129
	v_fmac_f32_e32 v88, v68, v128
	ds_read_b128 v[126:129], v39 offset:26624
	v_add_f32_e32 v83, v83, v88
	v_add_f32_e32 v88, v74, v83
	s_waitcnt lgkmcnt(11)
	v_mul_f32_e32 v83, v69, v133
	v_fmac_f32_e32 v83, v68, v132
	v_mul_f32_e32 v74, v71, v131
	v_fmac_f32_e32 v74, v70, v130
	ds_read_b128 v[130:133], v39 offset:30720
	v_add_f32_e32 v74, v74, v83
	v_add_f32_e32 v90, v37, v74
	s_waitcnt lgkmcnt(11)
	v_mul_f32_e32 v74, v69, v137
	v_fmac_f32_e32 v74, v68, v136
	v_mul_f32_e32 v37, v71, v135
	v_fmac_f32_e32 v37, v70, v134
	ds_read_b128 v[134:137], v39 offset:34816
	v_add_f32_e32 v37, v37, v74
	v_add_f32_e32 v92, v36, v37
	s_waitcnt lgkmcnt(11)
	v_mul_f32_e32 v36, v71, v139
	v_mul_f32_e32 v37, v69, v141
	v_fmac_f32_e32 v36, v70, v138
	v_fmac_f32_e32 v37, v68, v140
	ds_read_b128 v[138:141], v39 offset:38912
	v_add_f32_e32 v36, v36, v37
	v_add_f32_e32 v93, v35, v36
	s_waitcnt lgkmcnt(11)
	v_mul_f32_e32 v35, v71, v143
	v_mul_f32_e32 v36, v69, v145
	v_fmac_f32_e32 v35, v70, v142
	v_fmac_f32_e32 v36, v68, v144
	ds_read_b128 v[142:145], v39 offset:43008
	v_add_f32_e32 v35, v35, v36
	v_add_f32_e32 v94, v34, v35
	s_waitcnt lgkmcnt(11)
	v_mul_f32_e32 v35, v71, v147
	v_fmac_f32_e32 v35, v70, v146
	v_mul_f32_e32 v34, v69, v149
	v_fmac_f32_e32 v34, v68, v148
	ds_read_b128 v[146:149], v39 offset:47104
	v_add_f32_e32 v34, v35, v34
	v_add_f32_e32 v0, v0, v34
	s_waitcnt lgkmcnt(11)
	v_mul_f32_e32 v35, v67, v233
	v_fmac_f32_e32 v35, v66, v232
	v_mul_f32_e32 v34, v65, v235
	v_fmac_f32_e32 v34, v64, v234
	ds_read_b128 v[232:235], v39 offset:51200
	v_add_f32_e32 v34, v35, v34
	v_add_f32_e32 v91, v72, v34
	s_waitcnt lgkmcnt(11)
	v_mul_f32_e32 v35, v67, v237
	v_fmac_f32_e32 v35, v66, v236
	v_mul_f32_e32 v34, v65, v239
	v_fmac_f32_e32 v34, v64, v238
	ds_read_b128 v[236:239], v39 offset:55296
	v_add_f32_e32 v34, v35, v34
	v_add_f32_e32 v89, v73, v34
	s_waitcnt lgkmcnt(11)
	v_mul_f32_e32 v35, v67, v241
	v_fmac_f32_e32 v35, v66, v240
	v_mul_f32_e32 v34, v65, v243
	v_fmac_f32_e32 v34, v64, v242
	ds_read_b128 v[240:243], v39 offset:59392
	v_add_f32_e32 v34, v35, v34
	v_add_f32_e32 v83, v75, v34
	s_waitcnt lgkmcnt(11)
	v_mul_f32_e32 v35, v67, v245
	v_fmac_f32_e32 v35, v66, v244
	v_mul_f32_e32 v34, v65, v247
	v_fmac_f32_e32 v34, v64, v246
	ds_read_b128 v[244:247], v39 offset:63488
	v_add_f32_e32 v34, v35, v34
	v_add_f32_e32 v75, v77, v34
	s_waitcnt lgkmcnt(11)
	v_mul_f32_e32 v35, v67, v119
	v_fmac_f32_e32 v35, v66, v118
	v_mul_f32_e32 v34, v65, v121
	v_fmac_f32_e32 v34, v64, v120
	ds_read_b128 v[118:121], v39 offset:3072
	v_add_f32_e32 v34, v35, v34
	v_add_f32_e32 v72, v79, v34
	s_waitcnt lgkmcnt(11)
	v_mul_f32_e32 v35, v67, v123
	v_fmac_f32_e32 v35, v66, v122
	v_mul_f32_e32 v34, v65, v125
	v_fmac_f32_e32 v34, v64, v124
	ds_read_b128 v[122:125], v39 offset:7168
	v_add_f32_e32 v34, v35, v34
	v_add_f32_e32 v74, v81, v34
	s_waitcnt lgkmcnt(11)
	v_mul_f32_e32 v35, v67, v127
	v_fmac_f32_e32 v35, v66, v126
	v_mul_f32_e32 v34, v65, v129
	v_fmac_f32_e32 v34, v64, v128
	ds_read_b128 v[126:129], v39 offset:11264
	v_add_f32_e32 v34, v35, v34
	v_add_f32_e32 v73, v82, v34
	s_waitcnt lgkmcnt(11)
	v_mul_f32_e32 v35, v67, v131
	v_fmac_f32_e32 v35, v66, v130
	v_mul_f32_e32 v34, v65, v133
	v_fmac_f32_e32 v34, v64, v132
	ds_read_b128 v[130:133], v39 offset:15360
	v_add_f32_e32 v34, v35, v34
	v_add_f32_e32 v71, v80, v34
	s_waitcnt lgkmcnt(11)
	v_mul_f32_e32 v35, v67, v135
	v_fmac_f32_e32 v35, v66, v134
	v_mul_f32_e32 v34, v65, v137
	v_fmac_f32_e32 v34, v64, v136
	ds_read_b128 v[134:137], v39 offset:19456
	v_add_f32_e32 v34, v35, v34
	v_add_f32_e32 v70, v78, v34
	s_waitcnt lgkmcnt(11)
	v_mul_f32_e32 v35, v67, v139
	v_fmac_f32_e32 v35, v66, v138
	v_mul_f32_e32 v34, v65, v141
	v_fmac_f32_e32 v34, v64, v140
	ds_read_b128 v[138:141], v39 offset:23552
	v_add_f32_e32 v34, v35, v34
	v_add_f32_e32 v69, v76, v34
	s_waitcnt lgkmcnt(11)
	v_mul_f32_e32 v35, v67, v143
	v_fmac_f32_e32 v35, v66, v142
	v_mul_f32_e32 v34, v65, v145
	v_fmac_f32_e32 v34, v64, v144
	ds_read_b128 v[142:145], v39 offset:27648
	v_add_f32_e32 v34, v35, v34
	v_add_f32_e32 v68, v88, v34
	s_waitcnt lgkmcnt(11)
	v_mul_f32_e32 v35, v67, v147
	v_fmac_f32_e32 v35, v66, v146
	v_mul_f32_e32 v34, v65, v149
	v_fmac_f32_e32 v34, v64, v148
	ds_read_b128 v[146:149], v39 offset:31744
	v_add_f32_e32 v34, v35, v34
	v_add_f32_e32 v37, v90, v34
	s_waitcnt lgkmcnt(11)
	v_mul_f32_e32 v34, v67, v233
	v_mul_f32_e32 v35, v65, v235
	v_fmac_f32_e32 v34, v66, v232
	v_fmac_f32_e32 v35, v64, v234
	ds_read_b128 v[232:235], v39 offset:35840
	v_add_f32_e32 v34, v34, v35
	v_add_f32_e32 v36, v92, v34
	s_waitcnt lgkmcnt(11)
	v_mul_f32_e32 v34, v67, v237
	v_mul_f32_e32 v35, v65, v239
	v_fmac_f32_e32 v34, v66, v236
	v_fmac_f32_e32 v35, v64, v238
	ds_read_b128 v[236:239], v39 offset:39936
	v_add_f32_e32 v34, v34, v35
	v_add_f32_e32 v35, v93, v34
	s_waitcnt lgkmcnt(11)
; #define LAS __attribute__((address_space(3)))
; template <int CTRL> __device__ __forceinline__ float dpp_get(float v) { return __int_as_float(__builtin_amdgcn_update_dpp(0, __float_as_int(v), CTRL, 0xF, 0xF, false)); }
; __device__ __forceinline__ void ph_ln1(const Params& p, int l, LAS unsigned char* lds, const int wvid) {
;     ...
; #pragma unroll
;         for (int j = 0; j < 4; ++j)
; #pragma unroll
;             for (int e = 0; e < 16; ++e) { const f32x4 w = *(const LAS f32x4*)(rw + e * D + 256 * j + 4 * lane);
;                 lg[e] += (v[j][0] * w[0] + v[j][1] * w[1]) + (v[j][2] * w[2] + v[j][3] * w[3]); }
;         { const bool b3 = lane & 8, b2 = lane & 4, b1 = lane & 2, b0 = lane & 1;
;           float h8[8], h4[4], h2[2];
; #pragma unroll
;           for (int i = 0; i < 8; ++i) h8[i] = (b3 ? lg[i + 8] : lg[i]) + dpp_get<0x128>(b3 ? lg[i] : lg[i + 8]);
; #pragma unroll
;           for (int i = 0; i < 4; ++i) h4[i] = (b2 ? h8[i + 4] : h8[i]) + dpp_get<0x141>(b2 ? h8[i] : h8[i + 4]);
; #pragma unroll
;           for (int i = 0; i < 2; ++i) h2[i] = (b1 ? h4[i + 2] : h4[i]) + dpp_get<0x4E>(b1 ? h4[i] : h4[i + 2]);
;           float x = (b0 ? h2[1] : h2[0]) + dpp_get<0xB1>(b0 ? h2[0] : h2[1]);
;           x += __shfl_xor(x, 16); x += __shfl_xor(x, 32);
;           if (lane < 16) LG[(wave * 20 + k) * 16 + lane] = x; }
	v_mul_f32_e32 v34, v67, v241
	v_fmac_f32_e32 v34, v66, v240
	v_mul_f32_e32 v76, v65, v243
	v_fmac_f32_e32 v76, v64, v242
	ds_read_b128 v[240:243], v39 offset:44032
	v_add_f32_e32 v34, v34, v76
	v_add_f32_e32 v34, v94, v34
	s_waitcnt lgkmcnt(11)
	v_mul_f32_e32 v67, v67, v245
	v_mul_f32_e32 v65, v65, v247
	v_fmac_f32_e32 v67, v66, v244
	v_fmac_f32_e32 v65, v64, v246
	ds_read_b128 v[244:247], v39 offset:48128
	v_add_f32_e32 v64, v67, v65
	v_add_f32_e32 v0, v0, v64
	s_waitcnt lgkmcnt(11)
	v_mul_f32_e32 v65, v63, v119
	v_fmac_f32_e32 v65, v62, v118
	v_mul_f32_e32 v64, v61, v121
	v_fmac_f32_e32 v64, v60, v120
	ds_read_b128 v[118:121], v39 offset:52224
	v_add_f32_e32 v64, v65, v64
	s_waitcnt lgkmcnt(11)
	v_mul_f32_e32 v65, v63, v123
	v_mul_f32_e32 v66, v61, v125
	v_fmac_f32_e32 v65, v62, v122
	v_fmac_f32_e32 v66, v60, v124
	ds_read_b128 v[122:125], v39 offset:56320
	v_add_f32_e32 v65, v65, v66
	v_add_f32_e32 v64, v91, v64
	v_add_f32_e32 v65, v89, v65
	s_waitcnt lgkmcnt(11)
	v_mul_f32_e32 v66, v63, v127
	v_mul_f32_e32 v67, v61, v129
	v_fmac_f32_e32 v66, v62, v126
	v_fmac_f32_e32 v67, v60, v128
	ds_read_b128 v[126:129], v39 offset:60416
	v_add_f32_e32 v66, v66, v67
	v_add_f32_e32 v66, v83, v66
	s_waitcnt lgkmcnt(11)
	v_mul_f32_e32 v67, v63, v131
	v_fmac_f32_e32 v67, v62, v130
	v_mul_f32_e32 v76, v61, v133
	v_fmac_f32_e32 v76, v60, v132
	ds_read_b128 v[130:133], v39 offset:64512
	v_add_f32_e32 v67, v67, v76
	v_add_f32_e32 v67, v75, v67
	s_waitcnt lgkmcnt(11)
	v_mul_f32_e32 v75, v63, v135
	v_fmac_f32_e32 v75, v62, v134
	v_mul_f32_e32 v76, v61, v137
	v_fmac_f32_e32 v76, v60, v136
	v_add_f32_e32 v75, v75, v76
	v_add_f32_e32 v72, v72, v75
	s_waitcnt lgkmcnt(10)
	v_mul_f32_e32 v75, v63, v139
	v_fmac_f32_e32 v75, v62, v138
	v_mul_f32_e32 v76, v61, v141
	v_fmac_f32_e32 v76, v60, v140
	v_add_f32_e32 v75, v75, v76
	v_add_f32_e32 v74, v74, v75
	s_waitcnt lgkmcnt(9)
	v_mul_f32_e32 v75, v63, v143
	v_fmac_f32_e32 v75, v62, v142
	v_mul_f32_e32 v76, v61, v145
	v_fmac_f32_e32 v76, v60, v144
	v_add_f32_e32 v75, v75, v76
	v_add_f32_e32 v73, v73, v75
	s_waitcnt lgkmcnt(8)
	v_mul_f32_e32 v75, v63, v147
	v_fmac_f32_e32 v75, v62, v146
	v_mul_f32_e32 v76, v61, v149
	v_fmac_f32_e32 v76, v60, v148
	v_add_f32_e32 v75, v75, v76
	v_add_f32_e32 v71, v71, v75
	s_waitcnt lgkmcnt(7)
	v_mul_f32_e32 v75, v63, v233
	v_fmac_f32_e32 v75, v62, v232
	v_mul_f32_e32 v76, v61, v235
	v_fmac_f32_e32 v76, v60, v234
	v_add_f32_e32 v75, v75, v76
	v_add_f32_e32 v70, v70, v75
	s_waitcnt lgkmcnt(6)
	v_mul_f32_e32 v75, v63, v237
	v_fmac_f32_e32 v75, v62, v236
	v_mul_f32_e32 v76, v61, v239
	v_fmac_f32_e32 v76, v60, v238
	v_add_f32_e32 v75, v75, v76
	v_add_f32_e32 v69, v69, v75
	s_waitcnt lgkmcnt(5)
	v_mul_f32_e32 v75, v63, v241
	v_fmac_f32_e32 v75, v62, v240
	v_mul_f32_e32 v76, v61, v243
	v_fmac_f32_e32 v76, v60, v242
	v_add_f32_e32 v75, v75, v76
	v_add_f32_e32 v68, v68, v75
	s_waitcnt lgkmcnt(4)
	v_mul_f32_e32 v75, v63, v245
	v_fmac_f32_e32 v75, v62, v244
	v_mul_f32_e32 v76, v61, v247
	v_fmac_f32_e32 v76, v60, v246
	v_add_f32_e32 v75, v75, v76
	v_add_f32_e32 v75, v37, v75
	s_waitcnt lgkmcnt(3)
	v_mul_f32_e32 v37, v63, v119
	v_fmac_f32_e32 v37, v62, v118
	v_mul_f32_e32 v76, v61, v121
	v_fmac_f32_e32 v76, v60, v120
	v_add_f32_e32 v37, v37, v76
	v_add_f32_e32 v80, v36, v37
	s_waitcnt lgkmcnt(2)
	v_mul_f32_e32 v36, v63, v123
	v_mul_f32_e32 v37, v61, v125
	v_fmac_f32_e32 v36, v62, v122
	v_fmac_f32_e32 v37, v60, v124
	v_add_f32_e32 v36, v36, v37
	v_add_f32_e32 v81, v35, v36
	s_waitcnt lgkmcnt(1)
	v_mul_f32_e32 v35, v63, v127
	v_mul_f32_e32 v36, v61, v129
	v_fmac_f32_e32 v35, v62, v126
	v_fmac_f32_e32 v36, v60, v128
	v_add_f32_e32 v35, v35, v36
	v_add_f32_e32 v76, v34, v35
	s_waitcnt lgkmcnt(0)
	v_mul_f32_e32 v35, v63, v131
	v_fmac_f32_e32 v35, v62, v130
	v_mul_f32_e32 v34, v61, v133
	v_fmac_f32_e32 v34, v60, v132
	v_add_f32_e32 v34, v35, v34
	v_add_f32_e32 v0, v0, v34
	v_cndmask_b32_e32 v34, v70, v64, vcc
	v_cndmask_b32_e32 v35, v64, v70, vcc
	v_cndmask_b32_e32 v36, v65, v69, vcc
	v_cndmask_b32_e32 v37, v66, v68, vcc
	v_add_f32_dpp v34, v35, v34 row_ror:8 row_mask:0xf bank_mask:0xf bound_ctrl:1
	v_cndmask_b32_e32 v35, v69, v65, vcc
	v_cndmask_b32_e32 v60, v67, v75, vcc
	v_cndmask_b32_e32 v61, v72, v80, vcc
	v_add_f32_dpp v35, v36, v35 row_ror:8 row_mask:0xf bank_mask:0xf bound_ctrl:1
	v_cndmask_b32_e32 v36, v68, v66, vcc
	v_cndmask_b32_e32 v62, v74, v81, vcc
	v_cndmask_b32_e32 v63, v73, v76, vcc
	v_add_f32_dpp v36, v37, v36 row_ror:8 row_mask:0xf bank_mask:0xf bound_ctrl:1
	v_cndmask_b32_e32 v37, v75, v67, vcc
	s_nop 1
	v_add_f32_dpp v37, v60, v37 row_ror:8 row_mask:0xf bank_mask:0xf bound_ctrl:1
	v_cndmask_b32_e32 v60, v80, v72, vcc
	s_nop 1
	v_add_f32_dpp v60, v61, v60 row_ror:8 row_mask:0xf bank_mask:0xf bound_ctrl:1
	v_cndmask_b32_e32 v61, v81, v74, vcc
	s_nop 1
	v_add_f32_dpp v61, v62, v61 row_ror:8 row_mask:0xf bank_mask:0xf bound_ctrl:1
	v_cndmask_b32_e32 v62, v76, v73, vcc
	s_nop 1
	v_add_f32_dpp v62, v63, v62 row_ror:8 row_mask:0xf bank_mask:0xf bound_ctrl:1
	v_cndmask_b32_e32 v63, v0, v71, vcc
	v_cndmask_b32_e32 v0, v71, v0, vcc
	s_nop 1
	v_add_f32_dpp v0, v0, v63 row_ror:8 row_mask:0xf bank_mask:0xf bound_ctrl:1
	v_cndmask_b32_e64 v63, v60, v34, s[4:5]
	v_cndmask_b32_e64 v34, v34, v60, s[4:5]
	v_cndmask_b32_e64 v60, v61, v35, s[4:5]
	v_cndmask_b32_e64 v35, v35, v61, s[4:5]
	v_add_f32_dpp v34, v34, v63 row_half_mirror row_mask:0xf bank_mask:0xf bound_ctrl:1
	s_nop 0
	v_add_f32_dpp v35, v35, v60 row_half_mirror row_mask:0xf bank_mask:0xf bound_ctrl:1
	v_cndmask_b32_e64 v60, v62, v36, s[4:5]
	v_cndmask_b32_e64 v36, v36, v62, s[4:5]
	s_nop 1
	v_add_f32_dpp v36, v36, v60 row_half_mirror row_mask:0xf bank_mask:0xf bound_ctrl:1
	v_cndmask_b32_e64 v60, v0, v37, s[4:5]
	v_cndmask_b32_e64 v0, v37, v0, s[4:5]
	v_cndmask_b32_e64 v37, v36, v34, s[6:7]
	v_cndmask_b32_e64 v34, v34, v36, s[6:7]
	v_add_f32_dpp v0, v0, v60 row_half_mirror row_mask:0xf bank_mask:0xf bound_ctrl:1
	v_cndmask_b32_e64 v36, v0, v35, s[6:7]
	v_cndmask_b32_e64 v0, v35, v0, s[6:7]
	v_add_f32_dpp v34, v34, v37 quad_perm:[2,3,0,1] row_mask:0xf bank_mask:0xf bound_ctrl:1
	s_nop 0
	v_add_f32_dpp v0, v0, v36 quad_perm:[2,3,0,1] row_mask:0xf bank_mask:0xf bound_ctrl:1
	v_cndmask_b32_e64 v35, v0, v34, s[8:9]
	v_cndmask_b32_e64 v0, v34, v0, s[8:9]
	s_nop 1
	v_add_f32_dpp v0, v0, v35 quad_perm:[1,0,3,2] row_mask:0xf bank_mask:0xf bound_ctrl:1
	ds_bpermute_b32 v34, v43, v0
	s_waitcnt lgkmcnt(0)
	v_add_f32_e32 v0, v0, v34
	ds_bpermute_b32 v34, v85, v0
	s_and_saveexec_b64 s[0:1], s[10:11]
	s_cbranch_execz .LBB0_1073
	s_waitcnt lgkmcnt(0)
	v_add_f32_e32 v0, v0, v34
	ds_write_b32 v86, v0
	s_branch .LBB0_1073
